# P0 weight items rotated so expert-down weights are converted first
# speedup vs baseline: 1.0049x; 1.0049x over previous
.LBB0_54:
	s_lshl_b32 s3, s64, 3
	s_add_i32 s3, s3, s76
	s_lshl_b32 s12, s33, 3
	v_and_b32_e32 v2, 63, v38
	s_cmp_gt_i32 s3, 0x1963f
	v_lshlrev_b32_e32 v9, 3, v2
	s_barrier
	s_cbranch_scc1 .LBB0_87
	v_and_b32_e32 v10, 56, v9
	v_mov_b32_e32 v11, 0
	v_lshlrev_b32_e32 v12, 1, v10
	v_mov_b32_e32 v13, v11
	v_lshl_add_u64 v[12:13], s[28:29], 0, v[12:13]
	s_mov_b64 s[6:7], 0x2000000
	v_lshl_add_u64 v[12:13], v[12:13], 0, s[6:7]
	v_lshl_add_u64 v[28:29], s[28:29], 0, v[10:11]
	s_mov_b64 s[6:7], 0xb400000
	s_lshl_b32 s4, s76, 14
	v_lshrrev_b32_e32 v19, 3, v2
	v_lshl_add_u64 v[14:15], v[28:29], 0, s[6:7]
	s_mov_b64 s[6:7], 0x3200000
	s_add_i32 s8, s4, 0
	v_lshrrev_b32_e32 v4, 5, v2
	v_mul_u32_u24_e32 v1, 0x84, v10
	v_lshlrev_b32_e32 v3, 2, v19
	v_lshl_add_u64 v[16:17], v[28:29], 0, s[6:7]
	s_mov_b64 s[6:7], 0x1600000
	v_add3_u32 v23, s8, v1, v3
	v_and_b32_e32 v53, 16, v3
	v_lshl_add_u64 v[20:21], v[28:29], 0, s[6:7]
	s_mov_b64 s[6:7], 0xa00000
	v_mul_u32_u24_e32 v3, 0x84, v4
	v_and_b32_e32 v5, 31, v38
	v_bfe_u32 v52, v2, 3, 2
	v_lshl_add_u64 v[28:29], v[28:29], 0, s[6:7]
	v_or_b32_e32 v3, s4, v3
	s_lshl_b32 s4, s64, 8
	s_lshl_b32 s6, s76, 5
	v_lshlrev_b32_e32 v6, 2, v5
	v_or_b32_e32 v18, v53, v52
	v_mov_b32_e32 v7, v11
	s_add_i32 s14, s4, s6
	s_lshl_b32 s4, s64, 5
	s_lshl_b32 s6, s76, 2
	s_mov_b32 s5, 0
	v_add_u32_e32 v8, s8, v6
	s_movk_i32 s13, 0x84
	v_or_b32_e32 v25, 8, v19
	v_or_b32_e32 v27, 16, v19
	v_or_b32_e32 v39, 24, v19
	v_or_b32_e32 v22, 4, v18
	v_or_b32_e32 v24, 8, v18
	v_or_b32_e32 v26, 12, v18
	v_lshl_add_u64 v[30:31], s[22:23], 0, v[6:7]
	v_mov_b32_e32 v1, v4
	v_add3_u32 v54, v3, v6, 0
	s_lshl_b32 s15, s33, 8
	v_or_b32_e32 v55, 14, v4
	v_or_b32_e32 v56, 12, v4
	v_or_b32_e32 v57, 10, v4
	v_or_b32_e32 v58, 8, v4
	v_or_b32_e32 v59, 6, v4
	v_or_b32_e32 v60, 4, v4
	v_or_b32_e32 v61, 2, v4
	s_add_i32 s16, s4, s6
	s_lshl_b32 s17, s33, 5
	v_lshl_add_u64 v[32:33], s[38:39], 0, v[6:7]
	v_or_b32_e32 v62, 0xfffff80e, v4
	v_or_b32_e32 v63, 0xfffff80c, v4
	v_or_b32_e32 v64, 0xfffff80a, v4
	v_or_b32_e32 v65, 0xfffff808, v4
	v_or_b32_e32 v66, 0xfffff806, v4
	v_or_b32_e32 v67, 0xfffff804, v4
	v_or_b32_e32 v68, 0xfffff802, v4
	v_or_b32_e32 v69, 0xfffff800, v4
	s_movk_i32 s18, 0x7fff
	s_mov_b32 s19, 0xffff0000
	s_mov_b32 s20, 0xc3e00000
	s_movk_i32 s21, 0x3000
	v_mov_b32_e32 v70, 1
	v_mov_b32_e32 v71, 0x43e00000
	v_mov_b32_e32 v72, 0xc2317218
	v_mov_b32_e32 v73, 0xc2b8aa3b
	s_mov_b32 s98, s3
	s_branch .Lp0_remap
.LBB0_56:
	s_add_i32 s98, s98, s12
	s_cmp_gt_i32 s98, 0x1963f
	s_cbranch_scc1 .LBB0_87
.Lp0_remap:
	s_add_i32 s22, s98, 0x11400
	s_cmp_gt_i32 s22, 0x1963f
	s_cbranch_scc0 .Lp0_nowrap
	s_sub_i32 s22, s22, 0x19640
.Lp0_nowrap:
	s_lshl_b32 s14, s22, 5
	s_lshl_b32 s16, s22, 2
